# attention partial-O read-modify-write widened: two 16-byte loads/stores per lane via v_permlane16_swap pairs instead of four 8-byte ones (both attention loops)
# speedup vs baseline: 1.0029x; 1.0029x over previous
; __device__ __forceinline__ float opaque_f(float c) { float v = c; asm volatile("" : "+s"(v)); return v; }
; __device__ __forceinline__ void attn_group_mfma5(const bf16* QK, const float* bias2g, int ldil, int first, bf16* OACC, float* LSE, LAS unsigned char* lds, const int tid, const int bid, const int G) {
;     ...
;     const int wq = __builtin_amdgcn_readfirstlane(tid >> 6), lane = tid & 63, n = lane & 15, kq = lane >> 4;
;     const int Ls = SEQ >> ldil, lq4 = 4 - ldil, nq4m = (1 << lq4) - 1, dilm = (1 << ldil) - 1;
;     constexpr float SC = 0.125f * 1.4426950409f;
;     const float NEGBIG = opaque_f(-1e30f);
;     constexpr int NP = BATCH * HA * 16 / 2;
;     const int npp = (NP + G - 1) / G, ns = 2 * npp;
;     const bool remap = (G == 256);
;     constexpr int AT5_BUF = 2 * 32768 + 768;
; __global__ void __launch_bounds__(NTHREADS, 2) mk_fwd(Args args) {
;     ...
;             const int ldil = 2 * aux;
;             if (ldil < 4 && G * 8 == BATCH * HA * 16 / 2) attn_group_ring(P_BIG, P_BIAS + aux * 16 * 129, ldil, aux == 0, P_OACC, P_LSE, lds + RING_OFF, tid, bid, G);
;             else attn_group_mfma5(P_BIG, P_BIAS + aux * 16 * 129, ldil, aux == 0, P_OACC, P_LSE, lds + RING_OFF, tid, bid, G);
.LBB0_149:
	s_and_b64 vcc, exec, s[2:3]
	s_cbranch_vccz .LBB0_268
	s_lshl_b32 s43, s24, 1
	s_cmp_lt_u32 s24, 2
	s_cselect_b64 s[0:1], -1, 0
	s_cmpk_eq_i32 s88, 0x100
	s_cselect_b64 s[10:11], -1, 0
	s_cmpk_lg_i32 s88, 0x100
	s_cselect_b64 s[12:13], -1, 0
	s_and_b64 s[0:1], s[0:1], s[10:11]
	s_add_u32 s80, s96, 0xda00000
	v_mbcnt_lo_u32_b32 v69, -1, 0
	v_mbcnt_hi_u32_b32 v69, -1, v69
	s_addc_u32 s81, s97, 0
	v_add_u32_e32 v68, s30, v69
	s_mov_b64 s[2:3], -1
	s_andn2_b64 vcc, exec, s[0:1]
	s_waitcnt vmcnt(0)
	v_and_b32_e32 v66, 63, v69
	v_and_b32_e32 v67, 15, v69
	v_bfe_u32 v51, v69, 4, 2
	v_and_b32_e32 v112, 1, v51
	v_mul_u32_u24_e32 v112, 24, v112
	v_mov_b32_e32 v113, 0
	s_cbranch_vccz .LBB0_225
	s_mul_i32 s60, s24, 0x810
	s_lshl_b64 s[0:1], s[60:61], 2
	s_add_u32 s0, s96, s0
	s_addc_u32 s1, s97, s1
	s_add_u32 s14, s0, 0x140000
	s_addc_u32 s15, s1, 0
	s_abs_i32 s2, s88
	v_cvt_f32_u32_e32 v0, s2
	v_readfirstlane_b32 s0, v68
	s_sub_i32 s39, 4, s43
	s_ashr_i32 s1, s0, 6
	v_rcp_iflag_f32_e32 v0, v0
	s_lshl_b32 s0, -1, s39
	s_sub_i32 s4, 0, s2
	s_not_b32 s48, s0
	v_mul_f32_e32 v0, 0x4f7ffffe, v0
	v_cvt_u32_f32_e32 v0, v0
	s_lshl_b32 s0, -1, s43
	s_not_b32 s49, s0
	s_add_i32 s0, s88, 0x7ff
	v_readfirstlane_b32 s5, v0
	s_mul_i32 s4, s4, s5
	s_mul_hi_u32 s4, s5, s4
	s_xor_b32 s3, s0, s88
	s_abs_i32 s0, s0
	s_add_i32 s5, s5, s4
	s_mul_hi_u32 s4, s0, s5
	s_mul_i32 s5, s4, s2
	s_sub_i32 s0, s0, s5
	s_lshr_b32 s33, 0x800, s43
	s_ashr_i32 s3, s3, 31
	s_add_i32 s5, s4, 1
	s_sub_i32 s6, s0, s2
	s_cmp_ge_u32 s0, s2
	s_cselect_b32 s4, s5, s4
	s_cselect_b32 s0, s6, s0
	s_add_i32 s5, s4, 1
	s_cmp_ge_u32 s0, s2
	s_cselect_b32 s0, s5, s4
	s_xor_b32 s0, s0, s3
	s_sub_i32 s40, s0, s3
	s_cmp_gt_i32 s40, 0
	s_mov_b32 s50, 0xf149f2ca
	s_cselect_b64 s[2:3], -1, 0
	s_cmp_lt_i32 s40, 1
	s_cbranch_scc1 .LBB0_165
	s_mov_b64 s[4:5], -1
	s_and_b64 vcc, exec, s[12:13]
	s_cbranch_vccz .LBB0_154
	s_mul_i32 s0, s40, s90
	s_cbranch_execnz .LBB0_156
	s_branch .LBB0_155

; #define LAS __attribute__((address_space(3)))
; #define AT_SU(s_) (2 * AT_P((s_) >> 1) + ((s_) & 1))
; #define AT_FETCH_Q(su_) do { const int su__ = (su_); const bf16* qp_ = QK + ((((size_t)((su__ >> 8) * 16 + ((su__ >> 4) & 15)) << ldil) | ((su__ >> lq4) & dilm)) * Ls + ((su__ & nq4m) * 128 + 16 * wq + n)) * 64 + 8 * kq; \
;         qf[0] = *(const bf16x8s*)qp_; qf[1] = *(const bf16x8s*)(qp_ + 32); } while (0)
; #define AT_SU(s_) (2 * AT_P((s_) >> 1) + ((s_) & 1))
; #define AT_FETCH_Q(su_) do { const int su__ = (su_); const bf16* qp_ = QK + ((((size_t)((su__ >> 8) * 16 + ((su__ >> 4) & 15)) << ldil) | ((su__ >> lq4) & dilm)) * Ls + ((su__ & nq4m) * 128 + 16 * wq + n)) * 64 + 8 * kq; \
;         qf[0] = *(const bf16x8s*)qp_; qf[1] = *(const bf16x8s*)(qp_ + 32); tick += 2; } while (0)
; __device__ __forceinline__ void attn_group_mfma5(const bf16* QK, const float* bias2g, int ldil, int first, bf16* OACC, float* LSE, LAS unsigned char* lds, const int tid, const int bid, const int G) {
;     ...
;         const int su = AT_SU(s), q4 = su & nq4m, rr = (su >> lq4) & dilm, h = (su >> 4) & 15, b = su >> 8;
;         const LAS unsigned char* Kl = lds + (s & 1) * AT5_BUF; const LAS unsigned char* Vl = Kl + 32768; const LAS float* tab = (const LAS float*)(Kl + 65536);
;         const size_t rowq = (size_t)b * SEQ + ((size_t)(q4 * 128 + 16 * wq + n) << ldil) + rr;
;         f32x4 S[9];
; #pragma unroll
;         for (int kb = 0; kb < 9; ++kb) S[kb] = (f32x4){0.f, 0.f, 0.f, 0.f};
;         { const LAS unsigned char* kp0 = Kl + (16 * wq + n) * 128;
; #pragma unroll
;           for (int ks = 0; ks < 2; ++ks)
; #pragma unroll
;             for (int kb = 0; kb < 9; ++kb) S[kb] = __builtin_amdgcn_mfma_f32_16x16x32_bf16(*(const LAS bf16x8s*)(kp0 + 16 * kb * 128 + (((4 * ks + kq) ^ fl) * 16)), qf[ks], S[kb], 0, 0, 0); }
;         __builtin_amdgcn_sched_barrier(0);
;         if (more) AT_FETCH_Q(AT_SU(s + 1));
;         float lold = 0.f; v2u xo[4];
;         if (!first) { lold = LSE[rowq * 16 + h];
; #pragma unroll
;             for (int db = 0; db < 4; ++db) xo[db] = *(const v2u*)(OACC + rowq * D + h * 64 + 16 * db + 4 * kq); }
.LBB0_215:
	s_lshl_b32 s0, s42, 1
	s_or_b32 s0, s0, s36
	s_and_b32 s36, s0, s48
	s_ashr_i32 s8, s42, 7
	s_ashr_i32 s0, s0, s39
	s_ashr_i32 s9, s8, 31
	s_lshl_b32 s36, s36, 7
	s_and_b32 s0, s0, s49
	s_lshl_b64 s[8:9], s[8:9], 11
	v_add_u32_e32 v0, s36, v71
	v_ashrrev_i32_e32 v1, 31, v0
	s_add_u32 s8, s8, s0
	s_addc_u32 s9, s9, 0
	v_lshlrev_b64 v[0:1], s43, v[0:1]
	v_lshl_add_u64 v[0:1], s[8:9], 0, v[0:1]
	v_cndmask_b32_e64 v2, 0, 1, s[44:45]
	v_lshlrev_b64 v[52:53], 6, v[0:1]
	v_lshlrev_b64 v[0:1], 11, v[0:1]
	s_bfe_u32 s0, s42, 0x40003
	v_cmp_ne_u32_e64 s[8:9], 1, v2
	s_andn2_b64 vcc, exec, s[44:45]
	v_lshl_add_u64 v[62:63], s[52:53], 0, v[52:53]
	v_lshl_add_u64 v[60:61], s[46:47], 0, v[0:1]
	v_lshlrev_b32_e32 v58, 1, v50
	s_cbranch_vccnz .LBB0_217
	s_lshl_b32 s60, s0, 2
	v_lshl_add_u64 v[0:1], v[62:63], 0, s[60:61]
	s_lshl_b32 s60, s0, 7
	v_lshl_add_u64 v[52:53], v[60:61], 0, s[60:61]
	v_mov_b32_e32 v59, v3
	v_lshl_add_u64 v[52:53], v[52:53], 0, v[58:59]
	v_lshl_add_u64 v[114:115], v[52:53], 0, v[112:113]
	global_load_dword v59, v[0:1], off
	global_load_dwordx4 v[104:107], v[114:115], off
	global_load_dwordx4 v[108:111], v[114:115], off offset:64
	s_branch .LBB0_218
.LBB0_217:
	v_mov_b32_e32 v59, 0
	v_mov_b32_e32 v104, 0
	v_mov_b32_e32 v105, 0
	v_mov_b32_e32 v106, 0
	v_mov_b32_e32 v107, 0
	v_mov_b32_e32 v108, 0
	v_mov_b32_e32 v109, 0
	v_mov_b32_e32 v110, 0
	v_mov_b32_e32 v111, 0

; #define LAS __attribute__((address_space(3)))
; __device__ __forceinline__ unsigned cvtpk(float lo, float hi) { f32x2_t v = {lo, hi}; bf16x2_t b = __builtin_convertvector(v, bf16x2_t); return __builtin_bit_cast(unsigned, b); }
; __device__ __forceinline__ void attn_group_mfma5(const bf16* QK, const float* bias2g, int ldil, int first, bf16* OACC, float* LSE, LAS unsigned char* lds, const int tid, const int bid, const int G) {
;     ...
;         const float il = __builtin_amdgcn_rcpf(l); float lse = mx + __builtin_amdgcn_logf(l);
;         float wn = il, wo = 0.f;
;         if (!first) { const float mm = fmaxf(lold, lse), eo = __builtin_amdgcn_exp2f(lold - mm), en = __builtin_amdgcn_exp2f(lse - mm), inv = __builtin_amdgcn_rcpf(eo + en); wn = en * inv * il; wo = eo * inv; lse = mm + __builtin_amdgcn_logf(eo + en); }
;         if (kq == 0) LSE[rowq * 16 + h] = lse;
; #pragma unroll
;         for (int db = 0; db < 4; ++db) { const v2u x = xo[db]; v2u y;
;             y.x = cvtpk(wn * O[db][0] + wo * bflo(x.x), wn * O[db][1] + wo * bfhi(x.x)); y.y = cvtpk(wn * O[db][2] + wo * bflo(x.y), wn * O[db][3] + wo * bfhi(x.y));
;             *(v2u*)(OACC + rowq * D + h * 64 + 16 * db + 4 * kq) = y; }
;         if (more && tid < 192) ((LAS float*)(lds + ((s + 1) & 1) * AT5_BUF + 65536))[tid] = bv;
.LBB0_221:
	s_or_b64 exec, exec, s[8:9]
	s_waitcnt vmcnt(0)
	v_permlane16_swap_b32_e32 v104, v106
	v_permlane16_swap_b32_e32 v105, v107
	v_permlane16_swap_b32_e32 v108, v110
	v_permlane16_swap_b32_e32 v109, v111
	v_lshlrev_b32_e32 v30, 16, v104
	v_and_b32_e32 v31, 0xffff0000, v104
	v_pk_mul_f32 v[30:31], v[2:3], v[30:31] op_sel_hi:[0,1]
	v_pk_fma_f32 v[24:25], v[24:25], v[0:1], v[30:31] op_sel_hi:[1,0,1]
	v_lshlrev_b32_e32 v30, 16, v105
	v_and_b32_e32 v31, 0xffff0000, v105
	s_lshl_b32 s60, s0, 7
	v_pk_mul_f32 v[30:31], v[2:3], v[30:31] op_sel_hi:[0,1]
	v_lshl_add_u64 v[28:29], v[60:61], 0, s[60:61]
	v_mov_b32_e32 v59, v3
	v_pk_fma_f32 v[26:27], v[26:27], v[0:1], v[30:31] op_sel_hi:[1,0,1]
	v_lshl_add_u64 v[28:29], v[28:29], 0, v[58:59]
	v_lshl_add_u64 v[114:115], v[28:29], 0, v[112:113]
	v_cvt_pk_bf16_f32 v24, v24, v25
	v_cvt_pk_bf16_f32 v25, v26, v27
	v_lshlrev_b32_e32 v30, 16, v106
	v_and_b32_e32 v31, 0xffff0000, v106
	v_pk_mul_f32 v[30:31], v[2:3], v[30:31] op_sel_hi:[0,1]
	v_pk_fma_f32 v[20:21], v[20:21], v[0:1], v[30:31] op_sel_hi:[1,0,1]
	v_lshlrev_b32_e32 v30, 16, v107
	v_and_b32_e32 v31, 0xffff0000, v107
	v_pk_mul_f32 v[30:31], v[2:3], v[30:31] op_sel_hi:[0,1]
	v_pk_fma_f32 v[22:23], v[22:23], v[0:1], v[30:31] op_sel_hi:[1,0,1]
	v_cvt_pk_bf16_f32 v26, v20, v21
	v_cvt_pk_bf16_f32 v27, v22, v23
	s_nop 1
	v_permlane16_swap_b32_e32 v24, v26
	v_permlane16_swap_b32_e32 v25, v27
	global_store_dwordx4 v[114:115], v[24:27], off
	v_lshlrev_b32_e32 v20, 16, v108
	v_and_b32_e32 v21, 0xffff0000, v108
	v_pk_mul_f32 v[20:21], v[2:3], v[20:21] op_sel_hi:[0,1]
	v_pk_fma_f32 v[16:17], v[16:17], v[0:1], v[20:21] op_sel_hi:[1,0,1]
	v_lshlrev_b32_e32 v20, 16, v109
	v_and_b32_e32 v21, 0xffff0000, v109
	v_pk_mul_f32 v[20:21], v[2:3], v[20:21] op_sel_hi:[0,1]
	v_pk_fma_f32 v[18:19], v[18:19], v[0:1], v[20:21] op_sel_hi:[1,0,1]
	v_cvt_pk_bf16_f32 v16, v16, v17
	v_cvt_pk_bf16_f32 v17, v18, v19
	v_lshlrev_b32_e32 v20, 16, v110
	v_and_b32_e32 v21, 0xffff0000, v110
	v_pk_mul_f32 v[20:21], v[2:3], v[20:21] op_sel_hi:[0,1]
	v_pk_fma_f32 v[12:13], v[12:13], v[0:1], v[20:21] op_sel_hi:[1,0,1]
	v_lshlrev_b32_e32 v20, 16, v111
	v_and_b32_e32 v21, 0xffff0000, v111
	v_pk_mul_f32 v[20:21], v[2:3], v[20:21] op_sel_hi:[0,1]
	v_pk_fma_f32 v[0:1], v[14:15], v[0:1], v[20:21] op_sel_hi:[1,0,1]
	v_cvt_pk_bf16_f32 v18, v12, v13
	v_cvt_pk_bf16_f32 v19, v0, v1
	s_and_b64 s[0:1], s[6:7], s[54:55]
	s_nop 0
	v_permlane16_swap_b32_e32 v16, v18
	v_permlane16_swap_b32_e32 v17, v19
	global_store_dwordx4 v[114:115], v[16:19], off offset:64
	s_and_saveexec_b64 s[8:9], s[0:1]
	s_cbranch_execz .LBB0_184
	s_bitcmp1_b32 s77, 0
	s_cselect_b32 s0, 0x10300, 0
	s_add_i32 s0, s0, 0
	v_lshl_add_u32 v0, v68, 2, s0
	v_add_u32_e32 v0, 0x10000, v0
	ds_write_b32 v0, v70
	s_branch .LBB0_184

; #define LAS __attribute__((address_space(3)))
; #define AT_SU(s_) (2 * AT_P((s_) >> 1) + ((s_) & 1))
; #define AT_FETCH_Q(su_) do { const int su__ = (su_); const bf16* qp_ = QK + ((((size_t)((su__ >> 8) * 16 + ((su__ >> 4) & 15)) << ldil) | ((su__ >> lq4) & dilm)) * Ls + ((su__ & nq4m) * 128 + 16 * wq + n)) * 64 + 8 * kq; \
;         qf[0] = *(const bf16x8s*)qp_; qf[1] = *(const bf16x8s*)(qp_ + 32); } while (0)
; #define AT_SU(s_) (2 * AT_P((s_) >> 1) + ((s_) & 1))
; #define AT_FETCH_Q(su_) do { const int su__ = (su_); const bf16* qp_ = QK + ((((size_t)((su__ >> 8) * 16 + ((su__ >> 4) & 15)) << ldil) | ((su__ >> lq4) & dilm)) * Ls + ((su__ & nq4m) * 128 + 16 * wq + n)) * 64 + 8 * kq; \
;         qf[0] = *(const bf16x8s*)qp_; qf[1] = *(const bf16x8s*)(qp_ + 32); tick += 2; } while (0)
; __device__ __forceinline__ void attn_group_ring(const bf16* QK, const float* bias2g, int ldil, int first, bf16* OACC, float* LSE, LAS unsigned char* lds, const int tid, const int bid, const int G) {
;     ...
;         const int su = AT_SU(s), q4 = su & nq4m, rr = (su >> lq4) & dilm, h = (su >> 4) & 15, b = su >> 8;
;         const size_t rowq = (size_t)b * SEQ + ((size_t)(q4 * 128 + 16 * wq + n) << ldil) + rr;
;         f32x4 S[9];
; #pragma unroll
;         for (int kb = 0; kb < 9; ++kb) S[kb] = (f32x4){0.f, 0.f, 0.f, 0.f};
; #pragma unroll
;         for (int ks = 0; ks < 2; ++ks)
; #pragma unroll
;             for (int kb = 0; kb < 9; ++kb) { const int wrow = 16 * (wq + kb);
;                 const LAS unsigned char* kp = lds + ((a + (wrow >> 7)) & 3) * 32768 + ((wrow & 127) + n) * 128 + (((4 * ks + kq) ^ fl) * 16);
;                 S[kb] = __builtin_amdgcn_mfma_f32_16x16x32_bf16(*(const LAS bf16x8s*)kp, qf[ks], S[kb], 0, 0, 0); }
;         __builtin_amdgcn_sched_barrier(0);
;         if (more) AT_FETCH_Q(AT_SU(s + 1));
;         float lold = 0.f; v2u xo[4];
;         if (!first) { lold = LSE[rowq * 16 + h];
; #pragma unroll
;             for (int db = 0; db < 4; ++db) xo[db] = *(const v2u*)(OACC + rowq * D + h * 64 + 16 * db + 4 * kq); }
.LBB0_240:
	s_bfe_u32 s1, s87, 0x20001
	s_cmp_lt_u32 s87, 8
	s_cselect_b64 s[4:5], -1, 0
	v_cndmask_b32_e64 v0, 0, 1, s[4:5]
	v_cndmask_b32_e64 v2, 0, 1, s[6:7]
	v_readfirstlane_b32 s4, v0
	s_or_b32 s4, s49, s4
	s_lshl_b32 s5, s4, 7
	s_or_b32 s1, s5, s1
	s_or_b32 s1, s1, s45
	s_lshl_b32 s1, s1, 1
	s_and_b32 s5, s87, 1
	s_or_b32 s1, s1, s5
	s_and_b32 s70, s1, s47
	s_ashr_i32 s1, s1, s14
	s_and_b32 s71, s1, s48
	s_lshl_b32 s1, s70, 7
	s_ashr_i32 s5, s4, 31
	v_add_u32_e32 v0, s1, v64
	s_lshl_b64 s[4:5], s[4:5], 11
	v_ashrrev_i32_e32 v1, 31, v0
	s_or_b32 s4, s4, s71
	v_lshlrev_b64 v[0:1], s43, v[0:1]
	v_lshl_add_u64 v[0:1], s[4:5], 0, v[0:1]
	v_lshlrev_b64 v[52:53], 6, v[0:1]
	v_lshlrev_b64 v[0:1], 11, v[0:1]
	v_cmp_ne_u32_e64 s[4:5], 1, v2
	s_andn2_b64 vcc, exec, s[6:7]
	v_lshl_add_u64 v[60:61], s[8:9], 0, v[52:53]
	v_lshl_add_u64 v[52:53], v[50:51], 0, v[0:1]
	v_lshl_add_u64 v[114:115], v[52:53], 0, v[112:113]
	s_cbranch_vccnz .LBB0_242
	global_load_dword v84, v[60:61], off
	global_load_dwordx4 v[104:107], v[114:115], off
	global_load_dwordx4 v[108:111], v[114:115], off offset:64
	s_branch .LBB0_243
.LBB0_242:
	v_mov_b32_e32 v84, 0
	v_mov_b32_e32 v104, 0
	v_mov_b32_e32 v105, 0
	v_mov_b32_e32 v106, 0
	v_mov_b32_e32 v107, 0
	v_mov_b32_e32 v108, 0
	v_mov_b32_e32 v109, 0
	v_mov_b32_e32 v110, 0
	v_mov_b32_e32 v111, 0

; __device__ __forceinline__ unsigned cvtpk(float lo, float hi) { f32x2_t v = {lo, hi}; bf16x2_t b = __builtin_convertvector(v, bf16x2_t); return __builtin_bit_cast(unsigned, b); }
; __device__ __forceinline__ void attn_group_ring(const bf16* QK, const float* bias2g, int ldil, int first, bf16* OACC, float* LSE, LAS unsigned char* lds, const int tid, const int bid, const int G) {
;     ...
;         const float il = __builtin_amdgcn_rcpf(l); float lse = mx + __builtin_amdgcn_logf(l);
;         float wn = il, wo = 0.f;
;         if (!first) { const float mm = fmaxf(lold, lse), eo = __builtin_amdgcn_exp2f(lold - mm), en = __builtin_amdgcn_exp2f(lse - mm), inv = __builtin_amdgcn_rcpf(eo + en); wn = en * inv * il; wo = eo * inv; lse = mm + __builtin_amdgcn_logf(eo + en); }
;         if (kq == 0) LSE[rowq * 16 + h] = lse;
; #pragma unroll
;         for (int db = 0; db < 4; ++db) { const v2u x = xo[db]; v2u y;
;             y.x = cvtpk(wn * O[db][0] + wo * bflo(x.x), wn * O[db][1] + wo * bfhi(x.x)); y.y = cvtpk(wn * O[db][2] + wo * bflo(x.y), wn * O[db][3] + wo * bfhi(x.y));
;             *(v2u*)(OACC + rowq * D + h * 64 + 16 * db + 4 * kq) = y; }
;         tick += 5;
;         if (more) { const int an = ((s + 1) / R) * RH + ((s + 1) % R); AT_WAITH(an + 1); }
.LBB0_247:
	s_or_b64 exec, exec, s[4:5]
	s_waitcnt vmcnt(0)
	v_permlane16_swap_b32_e32 v104, v106
	v_permlane16_swap_b32_e32 v105, v107
	v_permlane16_swap_b32_e32 v108, v110
	v_permlane16_swap_b32_e32 v109, v111
	v_lshlrev_b32_e32 v28, 16, v104
	v_and_b32_e32 v29, 0xffff0000, v104
	v_pk_mul_f32 v[28:29], v[2:3], v[28:29] op_sel_hi:[0,1]
	v_pk_fma_f32 v[24:25], v[24:25], v[0:1], v[28:29] op_sel_hi:[1,0,1]
	v_lshlrev_b32_e32 v28, 16, v105
	v_and_b32_e32 v29, 0xffff0000, v105
	v_pk_mul_f32 v[28:29], v[2:3], v[28:29] op_sel_hi:[0,1]
	v_pk_fma_f32 v[26:27], v[26:27], v[0:1], v[28:29] op_sel_hi:[1,0,1]
	v_cvt_pk_bf16_f32 v24, v24, v25
	v_cvt_pk_bf16_f32 v25, v26, v27
	v_lshlrev_b32_e32 v28, 16, v106
	v_and_b32_e32 v29, 0xffff0000, v106
	v_pk_mul_f32 v[28:29], v[2:3], v[28:29] op_sel_hi:[0,1]
	v_pk_fma_f32 v[20:21], v[20:21], v[0:1], v[28:29] op_sel_hi:[1,0,1]
	v_lshlrev_b32_e32 v28, 16, v107
	v_and_b32_e32 v29, 0xffff0000, v107
	v_pk_mul_f32 v[28:29], v[2:3], v[28:29] op_sel_hi:[0,1]
	v_pk_fma_f32 v[22:23], v[22:23], v[0:1], v[28:29] op_sel_hi:[1,0,1]
	v_cvt_pk_bf16_f32 v26, v20, v21
	v_cvt_pk_bf16_f32 v27, v22, v23
	s_nop 1
	v_permlane16_swap_b32_e32 v24, v26
	v_permlane16_swap_b32_e32 v25, v27
	global_store_dwordx4 v[114:115], v[24:27], off
	v_lshlrev_b32_e32 v20, 16, v108
	v_and_b32_e32 v21, 0xffff0000, v108
	v_pk_mul_f32 v[20:21], v[2:3], v[20:21] op_sel_hi:[0,1]
	v_pk_fma_f32 v[16:17], v[16:17], v[0:1], v[20:21] op_sel_hi:[1,0,1]
	v_lshlrev_b32_e32 v20, 16, v109
	v_and_b32_e32 v21, 0xffff0000, v109
	v_pk_mul_f32 v[20:21], v[2:3], v[20:21] op_sel_hi:[0,1]
	v_pk_fma_f32 v[18:19], v[18:19], v[0:1], v[20:21] op_sel_hi:[1,0,1]
	v_cvt_pk_bf16_f32 v16, v16, v17
	v_cvt_pk_bf16_f32 v17, v18, v19
	v_lshlrev_b32_e32 v20, 16, v110
	v_and_b32_e32 v21, 0xffff0000, v110
	v_pk_mul_f32 v[20:21], v[2:3], v[20:21] op_sel_hi:[0,1]
	v_pk_fma_f32 v[12:13], v[12:13], v[0:1], v[20:21] op_sel_hi:[1,0,1]
	v_lshlrev_b32_e32 v20, 16, v111
	v_and_b32_e32 v21, 0xffff0000, v111
	v_pk_mul_f32 v[20:21], v[2:3], v[20:21] op_sel_hi:[0,1]
	v_pk_fma_f32 v[0:1], v[14:15], v[0:1], v[20:21] op_sel_hi:[1,0,1]
	v_cvt_pk_bf16_f32 v18, v12, v13
	v_cvt_pk_bf16_f32 v19, v0, v1
	s_andn2_b64 vcc, exec, s[10:11]
	s_add_i32 s41, s41, 5
	v_permlane16_swap_b32_e32 v16, v18
	v_permlane16_swap_b32_e32 v17, v19
	global_store_dwordx4 v[114:115], v[16:19], off offset:64
	s_cbranch_vccnz .LBB0_233
	s_lshr_b32 s0, s42, s50
	s_xor_b32 s1, s87, 2
	s_add_i32 s0, s0, s1
	s_and_b32 s0, s0, 3
	s_cmp_eq_u32 s0, 1
	s_cselect_b32 s1, s53, s52
	s_cmp_eq_u32 s0, 2
	s_cselect_b32 s1, s54, s1
	s_cmp_eq_u32 s0, 3
	s_cselect_b32 s0, s55, s1
	s_sub_i32 s0, s41, s0
	s_ashr_i32 s0, s0, 2
	s_cmp_gt_i32 s0, 0
	s_mov_b64 s[4:5], -1
	s_cbranch_scc0 .LBB0_265
	s_cmp_lt_i32 s0, 3
	s_cbranch_scc1 .LBB0_259
	s_cmp_lt_i32 s0, 4
	s_cbranch_scc1 .LBB0_256
	s_cmp_lg_u32 s0, 4
	s_cbranch_scc0 .LBB0_253
	s_waitcnt vmcnt(20)
	s_mov_b64 s[4:5], 0
